# baseline (speedup 1.0000x reference)
_Z9qsim_mainPKDF16_PK15HIP_vector_typeIfLj2EEPf:
	s_cmpk_gt_i32 s2, 0x3ff
	s_cbranch_scc1 .LBB1_11
	s_load_dwordx4 s[8:11], s[0:1], 0x0
	s_load_dwordx2 s[4:5], s[0:1], 0x10
	s_mul_i32 s1, s2, 56
	s_mul_hi_i32 s0, s2, 56
	v_mbcnt_lo_u32_b32 v2, -1, 0
	s_waitcnt lgkmcnt(0)
	s_add_u32 s6, s8, 0x20000
	s_addc_u32 s7, s9, 0
	s_add_u32 s20, s8, 0x80000
	s_addc_u32 s21, s9, 0
	s_add_u32 s12, s8, 0x38000
	s_addc_u32 s13, s9, 0
	s_add_i32 s22, s2, 0xfffffe00
	s_add_u32 s14, s4, s1
	s_addc_u32 s15, s5, s0
	s_mul_hi_i32 s0, s2, 0xa00
	s_mulk_i32 s2, 0xa00
	v_mbcnt_hi_u32_b32 v161, -1, v2
	s_add_u32 s10, s10, s2
	v_and_b32_e32 v2, 64, v161
	s_addc_u32 s11, s11, s0
	v_mov_b32_e32 v155, 0
	s_movk_i32 s23, 0x1000
	s_mov_b64 s[16:17], 0x28000
	v_mov_b32_e32 v1, 0x10000
	s_movk_i32 s24, 0x100
	v_mov_b32_e32 v158, 0x60
	v_mov_b32_e32 v159, 0x280
	v_mov_b32_e32 v160, 0x1280
	s_mov_b64 s[18:19], 0x40000
	s_mov_b32 s25, 0x40000
	v_xor_b32_e32 v162, 32, v161
	v_add_u32_e32 v163, 64, v2
	v_xor_b32_e32 v164, 16, v161
	v_mov_b32_e32 v165, 0x10a00
	v_and_b32_e32 v2, 63, v0
	v_lshlrev_b32_e32 v2, 4, v2
	v_add_u32_e32 v3, 0x1000, v2
	global_load_dwordx4 v[222:225], v2, s[6:7]
	global_load_dwordx4 v[226:229], v2, s[6:7] offset:1024
	global_load_dwordx4 v[230:233], v2, s[6:7] offset:2048
	global_load_dwordx4 v[234:237], v2, s[6:7] offset:3072
	global_load_dwordx4 v[238:241], v3, s[6:7]
	global_load_dwordx4 v[242:245], v3, s[6:7] offset:1024
	global_load_dwordx4 v[246:249], v3, s[6:7] offset:2048
	global_load_dwordx4 v[250:253], v3, s[6:7] offset:3072
	s_nop 0
	s_branch .LBB1_3
